# in-loop expert gate/up weight conversion inside the MLA attention tile loop (register transpose, 64-B store pieces), down projections via the work queue, conversion quota 3
# baseline (speedup 1.0000x reference)
; #define LAS __attribute__((address_space(3)))
; __device__ __forceinline__ int hw_wave_slot() { return (int)(__builtin_amdgcn_s_getreg((5 << 11) | 4) & 63u); }
; __device__ __forceinline__ unsigned xb_add(unsigned* p, unsigned v) { return __hip_atomic_fetch_add(p, v, __ATOMIC_RELAXED, __HIP_MEMORY_SCOPE_AGENT); }
; __device__ __forceinline__ unsigned xb_xcc_id() { return (unsigned)__builtin_amdgcn_s_getreg((3 << 11) | 20) & 0xFu; }
;     __device__ __forceinline__ unsigned char* ws() const { return *(unsigned char* const __attribute__((address_space(4)))*)(p + 232); }
;     __device__ __forceinline__ int ph_lo() const { return *(const __attribute__((address_space(4))) int*)(p + 240); }
;     __device__ __forceinline__ int ph_hi() const { return *(const __attribute__((address_space(4))) int*)(p + 244); }
; __device__ __forceinline__ KA fresh_ka() { kaptr p = (kaptr)__builtin_amdgcn_kernarg_segment_ptr(); asm volatile("" : "+s"(p)); return KA{p}; }
; __device__ __forceinline__ XcdBarrier xcd_barrier_post(unsigned* bar, volatile LAS unsigned* st) {
;     XcdBarrier b; b.bar = bar; b.x = xb_xcc_id(); b.st = st;
;     if (tid_x() == 0) (void)xb_add(&bar[XB_XCNT(b.x)], 1u);
;     return b;
; __global__ void __launch_bounds__(512, 2) mk_fwd(Args args) {
;     ...
;         const KA a = fresh_ka(); unsigned char* ws = a.ws();
;         LAS unsigned char* lds = (LAS unsigned char*)lds_raw;
;         for (int u = threadIdx.x; u < 128; u += 512) ((LAS unsigned*)(lds + MISC_OFF))[u] = 0u;
;         __syncthreads();
;         if ((threadIdx.x & 63) == 0) ((LAS int*)(lds + MISC_OFF))[64 + hw_wave_slot()] = (int)(threadIdx.x >> 6);
;         __syncthreads();
;         unsigned* ctl = (unsigned*)(ws + WS_CTL);
;         bar.bar = ctl + CW_BAR; bar.x = 0; bar.st = (volatile LAS unsigned*)(lds + MISC_OFF) + 8;
;         if (!MK_PER_PHASE) bar = xcd_barrier_post(ctl + CW_BAR, (volatile LAS unsigned*)(lds + MISC_OFF) + 8);
;         lo = a.ph_lo(); hi = a.ph_hi();
.LBB0_4:
	s_or_b64 exec, exec, s[4:5]
	s_add_u32 s78, s2, 0x4000
	s_waitcnt lgkmcnt(0)
	s_barrier
	s_addc_u32 s79, s3, 0
	s_getreg_b32 s2, hwreg(HW_REG_XCC_ID, 0, 4)
	s_getreg_b32 s3, hwreg(HW_REG_HW_ID, 0, 6)
	s_and_b32 s3, s3, 63
	s_lshl_b32 s3, s3, 2
	s_add_i32 s3, s3, 0
	s_add_i32 s3, s3, 0x23f00
	v_mov_b32_e32 v0, s3
	ds_read_b32 v0, v0
	s_and_b32 s30, s2, 15
	v_mbcnt_lo_u32_b32 v1, -1, 0
	v_mbcnt_hi_u32_b32 v1, -1, v1
	s_waitcnt lgkmcnt(0)
	v_readfirstlane_b32 s2, v0
	s_lshl_b32 s2, s2, 6
	v_sub_u32_e32 v0, 0, v1
	v_cmp_eq_u32_e32 vcc, s2, v0
	s_and_saveexec_b64 s[2:3], vcc
	s_cbranch_execz .LBB0_7
	s_mov_b64 s[4:5], exec
	v_mbcnt_lo_u32_b32 v0, s4, 0
	v_mbcnt_hi_u32_b32 v0, s5, v0
	v_cmp_eq_u32_e32 vcc, 0, v0
	s_and_b64 s[6:7], exec, vcc
	s_mov_b64 exec, s[6:7]
	s_cbranch_execz .LBB0_7
	s_lshl_b32 s6, s30, 8
	s_bcnt1_i32_b64 s4, s[4:5]
	v_mov_b32_e32 v0, s6
	v_mov_b32_e32 v1, s4
	global_atomic_add v0, v1, s[78:79] offset:1024
	v_mov_b32_e32 v0, 0x1c000
	v_mov_b32_e32 v1, 0x8200
	global_atomic_umax v0, v1, s[78:79]

;     __device__ __forceinline__ const float* in(int i) const { return *(const float* const __attribute__((address_space(4)))*)(p + 8 * i); }
;     __device__ __forceinline__ unsigned char* ws() const { return *(unsigned char* const __attribute__((address_space(4)))*)(p + 232); }
; __device__ __forceinline__ CvtDesc conv_expert_desc(const KA& a, unsigned char* ws, int q) {
;     const int l = q / Q_PER_L; int r = q - l * Q_PER_L;
;     unsigned char* wl = ws + WS_W + (size_t)l * W_LSTRIDE;
;     CvtDesc d; d.f8 = (MOE_FP8_LAST && (MOE_FP8_GU_ALL || l == NLAYER - 1)) ? 1 : 0;
;     if (MOE_FP8_LAST && MOE_FP8_DOWN_ALL && r >= 2 * Q_IG) d.f8 = 1;
;     const int eb = d.f8 ? 1 : 2;
;     if (r < 2 * Q_IG) { const int up = r >= Q_IG; if (up) r -= Q_IG; const int e = r >> 8, rr = r & 255, kb = rr >> 3, nb = rr & 7, n0 = nb * 64;
;         const float* src = e < 64 ? a.in(up ? 21 : 20) + ((size_t)l * 64 + e) * DM * FFE : a.in(up ? 24 : 23) + (size_t)l * DM * FFE;
;         d.src = src + (size_t)(kb * 64) * FFE + n0; d.N = FFE; d.dKB = DM * eb;
;         d.dst = wl + W_GU + ((size_t)e * 1024 * DM + (size_t)((n0 >> 7) * 256 + up * 128 + (n0 & 127)) * DM + kb * 64) * eb;
.LBB0_788:
	s_and_b32 s49, s28, 3
	s_lshr_b32 s46, s28, 2
	s_sub_u32 s46, s28, s46
	s_cmp_lg_u32 s49, 3
	s_cselect_b32 s50, 1, 0
	s_cmp_eq_u32 s28, 3
	s_cselect_b32 s46, 48, s46
	s_cselect_b32 s50, 1, s50
	s_lshl_b32 s49, s46, 2
	s_add_u32 s49, s49, s54
	s_cmp_lt_u32 s49, 0x80
	s_cselect_b32 s100, 1, 0
	s_sub_u32 s101, s49, 0xc0
	s_cmp_lt_u32 s101, 2
	s_cselect_b32 s100, 1, s100
	s_and_b32 s50, s50, s100
	s_cmp_eq_u32 s50, 0
	s_cbranch_scc1 .Lilc_proc
	s_lshr_b32 s55, s46, 4
	s_and_b32 s57, s49, 63
	s_lshl_b32 s101, s56, 6
	s_add_u32 s101, s101, s57
	s_cmp_eq_u32 s55, 3
	s_cselect_b32 s55, s54, s55
	s_cselect_b32 s100, 3, 0
	s_cselect_b32 s101, s56, s101
	s_cselect_b32 s57, 64, s57
	s_add_u32 s100, s100, s55
	s_lshl_b32 s100, s100, 3
	s_add_u32 s100, s100, 0xa0
	s_load_dwordx2 s[44:45], s[6:7], s100

; #define LAS __attribute__((address_space(3)))
;     __device__ __forceinline__ unsigned char* ws() const { return *(unsigned char* const __attribute__((address_space(4)))*)(p + 232); }
; __device__ __forceinline__ void moe_tables(Frame& F, const KA& a, int l, LAS int* pref, LAS int* cntL) {
;     const unsigned* cnt = (const unsigned*)(a.ws() + WS_CTL) + CW_CNT + l * 4096;
;     if (F.tid < 64) cntL[F.tid] = (int)cnt[64 * F.tid];
;     if (F.tid == 64) cntL[64] = NTOK;
;     __syncthreads();
.LBB0_1404:
	s_or_b64 exec, exec, s[0:1]
	s_mul_i32 s4, s6, 0xc300
	s_add_i32 s4, s4, 0x14500
	v_cmp_eq_u32_e32 vcc, 0, v2
	s_and_saveexec_b64 s[0:1], vcc
	v_mov_b32_e32 v0, 0x20000
	v_mov_b32_e32 v1, s4
	global_atomic_umax v0, v1, s[10:11]
	s_or_b64 exec, exec, s[0:1]
	s_load_dword s46, s[82:83], 0x0
	v_cmp_eq_u32_e32 vcc, 64, v2
	s_and_saveexec_b64 s[0:1], vcc
	s_cbranch_execz .LBB0_1406
	v_readlane_b32 s4, v254, 33
	v_mov_b32_e32 v1, 0x2000
	s_nop 0
	v_mov_b32_e32 v0, s4
	ds_write_b32 v0, v1
